# P2 prologue loads batched; barriers after in-projection and down-projection split (wave 0 polls and invalidates, LDS flag for the other waves); router front: only wave 0 polls the arrival counter
# speedup vs baseline: 1.0115x; 1.0115x over previous
; #define LAS __attribute__((address_space(3)))
; #define TID() (wave * 64 + lane_id_v())
; __global__ void __launch_bounds__(512, 2) hymba_fwd(Args args) {
;     ...
;         LAS float* btab = (LAS float*)(lds + 8 * 12288);
;         const int tid = TID(), lane = tid & 63;
;         {
;             LAS float* rb = (LAS float*)(lds + 8 * 12288 + NH * 396 * 4);
;             LAS float* mhs = rb + 512;
;             LAS unsigned char* kbl = (LAS unsigned char*)(mhs + 16);
;             static_assert(8 * 12288 + NH * 396 * 4 + 2048 + 64 + 400 <= 131072, "P2 table scratch below the MoE tables");
;             rb[tid] = args.rel_bias[tid];
;             if (tid < 396) kbl[tid] = kBucket[tid / 132][tid % 132];
;             float gq = fabsf(args.q_norm_g[lane]), gk = fabsf(args.k_norm_g[lane]);
; #pragma unroll
;             for (int o = 1; o < 64; o <<= 1) { gq = fmaxf(gq, __shfl_xor(gq, o)); gk = fmaxf(gk, __shfl_xor(gk, o)); }
;             __syncthreads();
;             if (tid < NH) { float mb = 0.f; for (int b = 0; b < 32; ++b) mb = fmaxf(mb, fabsf(rb[b * NH + tid])); mhs[tid] = 1.02f * C2 * 64.f * gq * gk + mb * LOG2E; }
.LBB0_204:
	s_mov_b32 s98, 0
	s_add_u32 s8, s26, 0x8000000
	s_addc_u32 s9, s27, 0
	s_add_u32 s70, s26, 0x1d000000
	s_addc_u32 s71, s27, 0
	s_cmp_lt_i32 s94, 3
	s_cselect_b64 s[0:1], -1, 0
	s_cmp_gt_i32 s95, 2
	s_cselect_b64 s[20:21], -1, 0
	s_and_b64 s[0:1], s[0:1], s[20:21]
	s_andn2_b64 vcc, exec, s[0:1]
	s_cbranch_vccnz .LBB0_468
	s_waitcnt vmcnt(0)
	v_mbcnt_lo_u32_b32 v0, -1, 0
	v_mbcnt_hi_u32_b32 v0, -1, v0
	v_mov_b32_e32 v2, s6
	v_add_u32_e32 v156, s93, v0
	v_mov_b32_e32 v3, s7
	v_ashrrev_i32_e32 v157, 31, v156
	v_lshl_add_u64 v[2:3], v[156:157], 2, v[2:3]
	global_load_dword v13, v[2:3], off
	s_movk_i32 s0, 0x18c
	v_lshl_add_u32 v1, v156, 2, 0
	v_add_u32_e32 v2, 0x1e300, v1
	v_cmp_gt_i32_e32 vcc, s0, v156
	s_and_saveexec_b64 s[0:1], vcc
	s_cbranch_execz .LBB0_207
	s_mov_b32 s6, 0x3e0f83e1
	v_mul_hi_i32 v3, v156, s6
	v_lshrrev_b32_e32 v4, 31, v3
	v_ashrrev_i32_e32 v3, 5, v3
	s_getpc_b64 s[6:7]
	s_add_u32 s6, s6, kBucket@rel32@lo+4
	s_addc_u32 s7, s7, kBucket@rel32@hi+12
	v_add_u32_e32 v3, v3, v4
	s_movk_i32 s20, 0x84
	v_mov_b64_e32 v[4:5], s[6:7]
	v_mad_i64_i32 v[4:5], s[6:7], v3, s20, v[4:5]
	v_mul_lo_u32 v3, v3, s20
	v_sub_u32_e32 v6, v156, v3
	v_ashrrev_i32_e32 v7, 31, v6
	v_lshl_add_u64 v[4:5], v[4:5], 0, v[6:7]
	global_load_ubyte v14, v[4:5], off
.LBB0_207:
	s_or_b64 exec, exec, s[0:1]
	v_and_b32_e32 v159, 63, v0
	v_lshlrev_b32_e32 v157, 2, v159
	global_load_dword v3, v157, s[42:43]
	global_load_dword v4, v157, s[44:45]
	s_waitcnt vmcnt(2)
	ds_write_b32 v2, v13
	v_cmp_gt_i32_e32 vcc, 0x18c, v156
	s_and_saveexec_b64 s[0:1], vcc
	v_add_u32_e32 v15, 0x1eb40, v156
	ds_write_b8 v15, v14
	s_or_b64 exec, exec, s[0:1]
	v_mbcnt_lo_u32_b32 v5, -1, 0
	v_mbcnt_hi_u32_b32 v5, -1, v5
	v_and_b32_e32 v6, 64, v5
	v_xor_b32_e32 v7, 1, v5
	v_add_u32_e32 v6, 64, v6
	v_cmp_lt_i32_e32 vcc, v7, v6
	v_xor_b32_e32 v8, 2, v5
	v_xor_b32_e32 v9, 4, v5
	v_cndmask_b32_e32 v7, v5, v7, vcc
	v_lshlrev_b32_e32 v198, 2, v7
	v_cmp_lt_i32_e32 vcc, v8, v6
	v_xor_b32_e32 v10, 8, v5
	v_xor_b32_e32 v11, 16, v5
	v_cndmask_b32_e32 v8, v5, v8, vcc
	v_lshlrev_b32_e32 v199, 2, v8
	v_cmp_lt_i32_e32 vcc, v9, v6
	v_xor_b32_e32 v12, 32, v5
	s_waitcnt lgkmcnt(0)
	v_cndmask_b32_e32 v9, v5, v9, vcc
	v_lshlrev_b32_e32 v200, 2, v9
	v_cmp_lt_i32_e32 vcc, v10, v6
	s_barrier
	s_nop 0
	v_cndmask_b32_e32 v9, v5, v10, vcc
	v_lshlrev_b32_e32 v201, 2, v9
	v_cmp_lt_i32_e32 vcc, v11, v6
	s_waitcnt vmcnt(1)
	v_and_b32_e32 v7, 0x7fffffff, v3
	s_waitcnt vmcnt(0)
	v_and_b32_e32 v13, 0x7fffffff, v4
	ds_bpermute_b32 v7, v198, v7
	ds_bpermute_b32 v13, v198, v13
	v_max_f32_e64 v3, |v3|, |v3|
	v_max_f32_e64 v4, |v4|, |v4|
	v_cndmask_b32_e32 v9, v5, v11, vcc
	s_waitcnt lgkmcnt(1)
	v_max_f32_e32 v7, v7, v7
	s_waitcnt lgkmcnt(0)
	v_max_f32_e32 v8, v13, v13
	v_max_f32_e32 v3, v3, v7
	v_max_f32_e32 v4, v4, v8
	ds_bpermute_b32 v7, v199, v3
	ds_bpermute_b32 v8, v199, v4
	v_lshlrev_b32_e32 v202, 2, v9
	v_cmp_lt_i32_e32 vcc, v12, v6
	s_waitcnt lgkmcnt(1)
	v_max_f32_e32 v7, v7, v7
	s_waitcnt lgkmcnt(0)
	v_max_f32_e32 v8, v8, v8
	v_max_f32_e32 v3, v3, v7
	v_max_f32_e32 v4, v4, v8
	ds_bpermute_b32 v7, v200, v3
	ds_bpermute_b32 v8, v200, v4
	v_cndmask_b32_e32 v5, v5, v12, vcc
	v_lshlrev_b32_e32 v203, 2, v5
	v_cmp_gt_i32_e32 vcc, 16, v156
	s_waitcnt lgkmcnt(1)
	v_max_f32_e32 v7, v7, v7
	s_waitcnt lgkmcnt(0)
	v_max_f32_e32 v8, v8, v8
	v_max_f32_e32 v3, v3, v7
	v_max_f32_e32 v4, v4, v8
	ds_bpermute_b32 v7, v201, v3
	ds_bpermute_b32 v8, v201, v4
	s_waitcnt lgkmcnt(1)
	v_max_f32_e32 v7, v7, v7
	s_waitcnt lgkmcnt(0)
	v_max_f32_e32 v8, v8, v8
	v_max_f32_e32 v3, v3, v7
	v_max_f32_e32 v4, v4, v8
	ds_bpermute_b32 v7, v202, v3
	ds_bpermute_b32 v8, v202, v4
	s_waitcnt lgkmcnt(1)
	v_max_f32_e32 v5, v7, v7
	s_waitcnt lgkmcnt(0)
	v_max_f32_e32 v6, v8, v8
	v_max_f32_e32 v3, v3, v5
	v_max_f32_e32 v5, v4, v6
	ds_bpermute_b32 v4, v203, v3
	ds_bpermute_b32 v6, v203, v5
	s_and_saveexec_b64 s[0:1], vcc
	s_cbranch_execz .LBB0_209
	s_waitcnt lgkmcnt(0)
	v_max_f32_e32 v8, v6, v6
	ds_read2_b32 v[6:7], v2 offset1:16
	v_max_f32_e32 v5, v5, v5
	v_max_f32_e32 v4, v4, v4
	v_max_f32_e32 v3, v3, v3
	v_max_f32_e32 v16, v5, v8
	v_max_f32_e32 v4, v3, v4
	s_waitcnt lgkmcnt(0)
	v_max3_f32 v3, |v6|, 0, |v7|
	ds_read2_b32 v[6:7], v2 offset0:32 offset1:48
	ds_read2_b32 v[8:9], v2 offset0:64 offset1:80
	ds_read2_b32 v[10:11], v2 offset0:96 offset1:112
	ds_read2_b32 v[12:13], v2 offset0:128 offset1:144
	ds_read2_b32 v[14:15], v2 offset0:160 offset1:176
	s_waitcnt lgkmcnt(4)
	v_max3_f32 v3, v3, |v6|, |v7|
	s_waitcnt lgkmcnt(3)
	v_max3_f32 v3, v3, |v8|, |v9|
	s_waitcnt lgkmcnt(2)
	v_max3_f32 v3, v3, |v10|, |v11|
	ds_read2_b32 v[6:7], v2 offset0:192 offset1:208
	ds_read2_b32 v[8:9], v2 offset0:224 offset1:240
	s_waitcnt lgkmcnt(3)
	v_max3_f32 v3, v3, |v12|, |v13|
	s_waitcnt lgkmcnt(2)
	v_max3_f32 v5, v3, |v14|, |v15|
	v_add_u32_e32 v14, 0x400, v2
	ds_read2_b32 v[2:3], v14 offset1:16
	ds_read2_b32 v[10:11], v14 offset0:32 offset1:48
	ds_read2_b32 v[12:13], v14 offset0:64 offset1:80
	s_waitcnt lgkmcnt(4)
	v_max3_f32 v5, v5, |v6|, |v7|
	s_waitcnt lgkmcnt(3)
	v_max3_f32 v5, v5, |v8|, |v9|
	s_waitcnt lgkmcnt(2)
	v_max3_f32 v2, v5, |v2|, |v3|
	s_waitcnt lgkmcnt(1)
	v_max3_f32 v2, v2, |v10|, |v11|
	s_waitcnt lgkmcnt(0)
	v_max3_f32 v5, v2, |v12|, |v13|
	ds_read2_b32 v[2:3], v14 offset0:96 offset1:112
	ds_read2_b32 v[6:7], v14 offset0:128 offset1:144
	ds_read2_b32 v[8:9], v14 offset0:160 offset1:176
	ds_read2_b32 v[10:11], v14 offset0:192 offset1:208
	ds_read2_b32 v[12:13], v14 offset0:224 offset1:240
	s_waitcnt lgkmcnt(4)
	v_max3_f32 v2, v5, |v2|, |v3|
	s_waitcnt lgkmcnt(3)
	v_max3_f32 v2, v2, |v6|, |v7|
	s_waitcnt lgkmcnt(2)
	v_max3_f32 v2, v2, |v8|, |v9|
	s_waitcnt lgkmcnt(1)
	v_max3_f32 v2, v2, |v10|, |v11|
	s_mov_b32 s6, 0x413c5bb7
	s_waitcnt lgkmcnt(0)
	v_max3_f32 v5, v2, |v12|, |v13|
	s_mov_b32 s7, 0x3fb8aa3b
	v_pk_mul_f32 v[2:3], v[4:5], s[6:7]
	v_add_u32_e32 v1, 0x1eb00, v1
	v_fmac_f32_e32 v3, v16, v2
	ds_write_b32 v1, v3

; __global__ void __launch_bounds__(512, 2) hymba_fwd(Args args) {
;     ...
;             for (int hs = 0; hs < 2 * nsteps; ++hs) {
;                 const bool doA = (((hs & 1) == 0) == (wave < 4));
;                 if (doA) { if (ia < nA) { const int a = bx + ia * G; const int blk = a >> 4, h = a & 15;
;                         attn_wave(Qb, Kb, Vb, MIX, h, 256 * blk + wave, vbuf, btab + h * 396, lane); ++ia; } }
.LBB0_214:
	s_and_b32 s0, s83, 1
	v_cmp_ne_u32_e32 vcc, s0, v223
	s_mov_b64 s[6:7], -1
	s_cbranch_vccnz .LBB0_234
	s_cmp_ge_i32 s82, s69
	s_mov_b32 s0, s82
	s_cbranch_scc1 .LBB0_233
	s_cmp_lg_u32 s98, 0
	s_cbranch_scc1 .Lp2gb_passed
	s_mov_b32 s99, 0
	s_cmp_lg_u32 s92, 0
	s_cbranch_scc1 .Lp2gb_follow
	v_mov_b32_e32 v21, 0x22604
	ds_read_b32 v233, v21
	v_mov_b32_e32 v21, 0x3000
	global_load_dword v22, v21, s[26:27] offset:1024 sc1
	s_waitcnt vmcnt(0) lgkmcnt(0)
	v_mul_u32_u24_e32 v233, 2, v233
	s_branch .Lp2gb_chk
.Lp2gb_spin:
	s_sleep 1
	global_load_dword v22, v21, s[26:27] offset:1024 sc1
	s_waitcnt vmcnt(0)
.Lp2gb_chk:
	v_cmp_ge_u32_e32 vcc, v22, v233
	s_cbranch_vccnz .Lp2gb_lead_done
	s_add_i32 s99, s99, 1
	s_cmp_lt_u32 s99, 0x8000
	s_cbranch_scc1 .Lp2gb_spin

; __global__ void __launch_bounds__(512, 2) hymba_fwd(Args args) {
;     ...
;                 if (doA) { if (ia < nA) { const int a = bx + ia * G; const int blk = a >> 4, h = a & 15;
;                         attn_wave(Qb, Kb, Vb, MIX, h, 256 * blk + wave, vbuf, btab + h * 396, lane); ++ia; } }
.Lp2gb_fdone:
.Lp2gb_done:
	s_mov_b32 s98, 1

; __global__ void __launch_bounds__(512, 2) hymba_fwd(Args args) {
;     ...
;         for (int tile = bx; tile < NTILE; tile += G) {
;             const int t0 = 32 * tile;
;             {
;                 const bf16* xp = X1B + (size_t)(t0 + li) * DM + 256 * wave + 8 * kg;
.LBB0_553:
	s_lshl_b32 s33, s66, 5
	s_lshr_b32 s16, s66, 3
	s_lshl_b32 s16, s16, 6
	s_add_i32 s16, s16, 0x6000
	s_add_u32 s20, s26, s16
	s_addc_u32 s21, s27, 0
	v_mov_b32_e32 v0, 0
	s_mov_b32 s16, 0
	s_cmp_lg_u32 s92, 0
	s_cbranch_scc1 .Lms_done

; __global__ void __launch_bounds__(512, 2) hymba_fwd(Args args) {
;     ...
;             __syncthreads();
;             for (int idx = tid; idx < 32 * 48; idx += 512) { float a = 0.f;
; #pragma unroll
;                 for (int w8 = 0; w8 < 8; ++w8) a += part[w8 * 1536 + idx];
;                 logit[idx] = a; }
;             if (tid < 32) { float a = 0.f;
; #pragma unroll
;                 for (int w8 = 0; w8 < 8; ++w8) a += ssp[w8 * 32 + tid];
;                 const float r = __builtin_amdgcn_rsqf(a * (1.f / DM) + NORM_EPS); rsl[tid] = r; rstd_g[t0 + tid] = r; }
;             __syncthreads();
.Lms_done:
	s_barrier
	s_lshl_b32 s16, s92, 13
	s_add_i32 s16, s16, s33
	s_mul_i32 s17, s16, 0xc0
	s_add_u32 s20, s26, 0x15000000
	s_addc_u32 s21, s27, 0
	s_add_u32 s20, s20, s17
	s_addc_u32 s21, s21, 0
	v_mbcnt_lo_u32_b32 v0, -1, 0
	v_mbcnt_hi_u32_b32 v0, -1, v0
	v_lshlrev_b32_e32 v1, 4, v0
	global_load_dwordx4 v[8:11], v1, s[20:21] sc0 sc1
	global_load_dwordx4 v[12:15], v1, s[20:21] offset:1024 sc0 sc1
	global_load_dwordx4 v[16:19], v1, s[20:21] offset:2048 sc0 sc1
	global_load_dwordx4 v[20:23], v1, s[20:21] offset:3072 sc0 sc1
	s_add_u32 s20, s20, 0x1000
	s_addc_u32 s21, s21, 0
	global_load_dwordx4 v[24:27], v1, s[20:21] sc0 sc1
	global_load_dwordx4 v[28:31], v1, s[20:21] offset:1024 sc0 sc1
	s_lshl_b32 s17, s16, 2
	s_add_u32 s20, s26, 0x16000000
	s_addc_u32 s21, s27, 0
	s_add_u32 s20, s20, s17
	s_addc_u32 s21, s21, 0
	v_lshlrev_b32_e32 v2, 2, v0
	global_load_dword v3, v2, s[20:21] sc0 sc1
	s_mul_i32 s17, s92, 0x1800
	v_add_u32_e32 v4, s17, v1
	s_lshl_b32 s17, s92, 7
	v_add_u32_e32 v5, s17, v2
	v_mov_b32_e32 v6, 0x33800000
	v_mov_b32_e32 v7, 0x37800000
	s_waitcnt vmcnt(0)
	v_cvt_f32_i32_e32 v8, v8
	v_cvt_f32_i32_e32 v9, v9
	v_cvt_f32_i32_e32 v10, v10
	v_cvt_f32_i32_e32 v11, v11
	v_cvt_f32_i32_e32 v12, v12
	v_cvt_f32_i32_e32 v13, v13
	v_cvt_f32_i32_e32 v14, v14
	v_cvt_f32_i32_e32 v15, v15
	v_cvt_f32_i32_e32 v16, v16
	v_cvt_f32_i32_e32 v17, v17
	v_cvt_f32_i32_e32 v18, v18
	v_cvt_f32_i32_e32 v19, v19
	v_cvt_f32_i32_e32 v20, v20
	v_cvt_f32_i32_e32 v21, v21
	v_cvt_f32_i32_e32 v22, v22
	v_cvt_f32_i32_e32 v23, v23
	v_cvt_f32_i32_e32 v24, v24
	v_cvt_f32_i32_e32 v25, v25
	v_cvt_f32_i32_e32 v26, v26
	v_cvt_f32_i32_e32 v27, v27
	v_cvt_f32_i32_e32 v28, v28
	v_cvt_f32_i32_e32 v29, v29
	v_cvt_f32_i32_e32 v30, v30
	v_cvt_f32_i32_e32 v31, v31
	v_mul_f32_e32 v8, v8, v6
	v_mul_f32_e32 v9, v9, v6
	v_mul_f32_e32 v10, v10, v6
	v_mul_f32_e32 v11, v11, v6
	v_mul_f32_e32 v12, v12, v6
	v_mul_f32_e32 v13, v13, v6
	v_mul_f32_e32 v14, v14, v6
	v_mul_f32_e32 v15, v15, v6
	v_mul_f32_e32 v16, v16, v6
	v_mul_f32_e32 v17, v17, v6
	v_mul_f32_e32 v18, v18, v6
	v_mul_f32_e32 v19, v19, v6
	v_mul_f32_e32 v20, v20, v6
	v_mul_f32_e32 v21, v21, v6
	v_mul_f32_e32 v22, v22, v6
	v_mul_f32_e32 v23, v23, v6
	v_mul_f32_e32 v24, v24, v6
	v_mul_f32_e32 v25, v25, v6
	v_mul_f32_e32 v26, v26, v6
	v_mul_f32_e32 v27, v27, v6
	v_mul_f32_e32 v28, v28, v6
	v_mul_f32_e32 v29, v29, v6
	v_mul_f32_e32 v30, v30, v6
	v_mul_f32_e32 v31, v31, v6
	v_cvt_f32_i32_e32 v3, v3
	s_nop 0
	v_mul_f32_e32 v3, v3, v7
	ds_write_b128 v4, v[8:11]
	ds_write_b128 v4, v[12:15] offset:1024
	ds_write_b128 v4, v[16:19] offset:2048
	ds_write_b128 v4, v[20:23] offset:3072
	ds_write_b128 v4, v[24:27] offset:4096
	ds_write_b128 v4, v[28:31] offset:5120
	s_mov_b32 exec_lo, -1
	s_mov_b32 exec_hi, 0
	ds_write_b32 v5, v3 offset:55296
	s_mov_b64 exec, -1
	s_waitcnt lgkmcnt(0)
	s_barrier
	s_and_saveexec_b64 s[12:13], s[14:15]
	s_cbranch_execz .LBB0_572
	s_mov_b64 s[20:21], -1
	v_mov_b32_e32 v1, v152
	s_and_saveexec_b64 s[16:17], s[18:19]
	s_cbranch_execz .LBB0_569
	v_mov_b32_e32 v2, 0
	s_and_saveexec_b64 s[20:21], s[6:7]
	s_cbranch_execz .LBB0_565
	s_mov_b32 s42, 0
	s_mov_b64 s[46:47], 0
	v_mov_b32_e32 v0, v179
	v_mov_b32_e32 v1, v176

; __device__ __forceinline__ unsigned xb_ld(unsigned* p)              { return __hip_atomic_load(p, __ATOMIC_RELAXED, __HIP_MEMORY_SCOPE_AGENT); }
; __device__ __forceinline__ unsigned xb_add(unsigned* p, unsigned v) { return __hip_atomic_fetch_add(p, v, __ATOMIC_RELAXED, __HIP_MEMORY_SCOPE_AGENT); }
; #define XB_SPIN(cond, bar) do { unsigned _sp = 0; while (cond) { __builtin_amdgcn_s_sleep(1); \
;     if ((++_sp & 255u) == 0u) { if (xb_ld(&(bar)[XB_TMO])) break; if (_sp > XB_SPIN_CAP) { atomicAdd(&(bar)[XB_TMO], 1u); break; } } } } while (0)
; __device__ __forceinline__ void xcd_barrier(const XcdBarrier& b, const int tid) {
;     ...
;         const unsigned old = xb_add(&bar[XB_XSUB(b.x)], 1u);
;         const unsigned gen = old / nloc;
;         if (old + 1u == (gen + 1u) * nloc) {
;             __builtin_amdgcn_fence(__ATOMIC_RELEASE, "agent");
;             asm volatile("s_waitcnt vmcnt(0)" ::: "memory");
;             const unsigned og = xb_add(&bar[XB_TOP], 1u);
;             const unsigned tg = og / nx;
;             if (og + 1u == (tg + 1u) * nx) xb_add(&bar[XB_TOPGEN], 1u);
;             else XB_SPIN(xb_ld(&bar[XB_TOPGEN]) == tg, bar);
;             __builtin_amdgcn_fence(__ATOMIC_ACQUIRE, "agent");
;             xb_add(&bar[XB_XGEN(b.x)], 1u);
;             asm volatile("s_waitcnt vmcnt(0)" ::: "memory");
.LBB0_874:
	s_or_b64 exec, exec, s[10:11]
	v_cvt_f32_u32_e32 v4, v2
	s_waitcnt vmcnt(0)
	v_readfirstlane_b32 s8, v3
	v_sub_u32_e32 v3, 0, v2
	v_rcp_iflag_f32_e32 v4, v4
	v_add_u32_e32 v5, s8, v1
	v_mul_f32_e32 v4, 0x4f7ffffe, v4
	v_cvt_u32_f32_e32 v4, v4
	v_mul_lo_u32 v1, v3, v4
	v_mul_hi_u32 v1, v4, v1
	v_add_u32_e32 v1, v4, v1
	v_mul_hi_u32 v1, v5, v1
	v_mul_lo_u32 v3, v1, v2
	v_sub_u32_e32 v3, v5, v3
	v_add_u32_e32 v4, 1, v1
	v_cmp_ge_u32_e32 vcc, v3, v2
	s_nop 1
	v_cndmask_b32_e32 v1, v1, v4, vcc
	v_sub_u32_e32 v4, v3, v2
	v_cndmask_b32_e32 v3, v3, v4, vcc
	v_add_u32_e32 v4, 1, v1
	v_cmp_ge_u32_e32 vcc, v3, v2
	v_add_u32_e32 v3, 1, v5
	s_nop 0
	v_cndmask_b32_e32 v1, v1, v4, vcc
	v_mul_lo_u32 v4, v2, v1
	v_add_u32_e32 v2, v4, v2
	s_waitcnt lgkmcnt(0)
	v_add_u32_e32 v4, 1, v1
	v_mul_lo_u32 v4, v4, v0
	v_mov_b32_e32 v5, 0x3000
	v_cmp_ne_u32_e32 vcc, v3, v2
	s_cbranch_vccnz .Lgb6_out
	buffer_wbl2 sc1
	s_waitcnt vmcnt(0) lgkmcnt(0)
	v_mov_b32_e32 v2, 1
	global_atomic_add v5, v2, s[26:27] offset:1024
.Lgb6_out:
	s_waitcnt vmcnt(0)

; __device__ __forceinline__ int lane_id_v() { int l; asm volatile("v_mbcnt_lo_u32_b32 %0, -1, 0\n\tv_mbcnt_hi_u32_b32 %0, -1, %0" : "=v"(l)); return l; }
; __global__ void __launch_bounds__(512, 2) hymba_fwd(Args args) {
;     ...
;         if (IN(7)) {
;             const int lane = lane_id_v();
;             const int* tokpos = (const int*)(ws + WS_TOKPOS);
;             for (int tq = gw; tq < SEQ; tq += 4 * NGW) {
;             int cc0[4], cc1[4];
; #pragma unroll
;             for (int k = 0; k < 4; ++k) { const int t = tq + k * NGW; cc0[k] = 0; cc1[k] = 0; if (t < SEQ) { cc0[k] = tokpos[2 * t]; cc1[k] = tokpos[2 * t + 1]; } }
.LBB0_909:
	s_mov_b32 s98, 0
	s_cmp_lt_i32 s94, 8
	s_cselect_b64 s[0:1], -1, 0
	s_cmp_gt_i32 s95, 7
	s_cselect_b64 s[6:7], -1, 0
	s_and_b64 s[0:1], s[0:1], s[6:7]
	s_andn2_b64 vcc, exec, s[0:1]
	s_cbranch_vccnz .LBB0_929
	s_cmpk_gt_i32 s34, 0x1fff
	s_waitcnt vmcnt(0)
	v_mbcnt_lo_u32_b32 v8, -1, 0
	v_mbcnt_hi_u32_b32 v8, -1, v8
	s_cbranch_scc1 .LBB0_929
	s_add_u32 s19, s26, 0x300000
	s_addc_u32 s30, s27, 0
	s_lshl_b32 s0, s2, 4
	s_lshl_b32 s1, s92, 1
	s_add_i32 s2, s0, s1
	s_add_i32 s0, s34, s90
	v_ashrrev_i32_e32 v9, 31, v8
	s_ashr_i32 s1, s0, 31
	v_lshlrev_b64 v[0:1], 4, v[8:9]
	s_lshl_b32 s6, s3, 5
	v_lshlrev_b64 v[4:5], 3, v[8:9]
	v_lshl_add_u64 v[8:9], v[8:9], 2, s[4:5]
	s_lshl_b32 s31, s3, 6
	s_lshl_b32 s33, s3, 4
	s_lshl_b64 s[4:5], s[0:1], 13
	s_add_u32 s4, s24, s4
	s_addc_u32 s5, s25, s5
	s_ashr_i32 s7, s6, 31
	s_ashr_i32 s35, s34, 31
	s_lshl_b64 s[8:9], s[6:7], 13
	s_lshl_b64 s[10:11], s[34:35], 12
	s_add_u32 s10, s26, s10
	s_addc_u32 s11, s27, s11
	s_lshl_b64 s[12:13], s[6:7], 12
	s_lshl_b64 s[0:1], s[0:1], 12
	s_add_u32 s14, s26, s0
	s_addc_u32 s15, s27, s1
	s_lshl_b64 s[0:1], s[34:35], 13
	s_add_u32 s16, s24, s0
	v_lshl_add_u64 v[2:3], s[24:25], 0, v[0:1]
	v_lshl_add_u64 v[6:7], s[38:39], 0, v[4:5]
	s_mul_i32 s36, s3, 24
	s_mul_i32 s37, s3, 48
	s_addc_u32 s17, s25, s1
	v_mov_b32_e32 v48, 0
	s_add_i32 s7, 0, 0x22400
	s_mov_b32 s35, 0x5000000
	s_mov_b32 s18, 0x3d800000
	s_movk_i32 s38, 0x1000
	v_mov_b32_e32 v49, 2
	s_branch .LBB0_913

; __device__ __forceinline__ unsigned xb_ld(unsigned* p)              { return __hip_atomic_load(p, __ATOMIC_RELAXED, __HIP_MEMORY_SCOPE_AGENT); }
; #define XB_SPIN(cond, bar) do { unsigned _sp = 0; while (cond) { __builtin_amdgcn_s_sleep(1); \
;     if ((++_sp & 255u) == 0u) { if (xb_ld(&(bar)[XB_TMO])) break; if (_sp > XB_SPIN_CAP) { atomicAdd(&(bar)[XB_TMO], 1u); break; } } } } while (0)
; __device__ __forceinline__ void xcd_barrier(const XcdBarrier& b, const int tid) {
;     ...
;             XB_SPIN(xb_ld(&bar[XB_XGEN(b.x)]) == gen, bar);
;             __builtin_amdgcn_fence(__ATOMIC_ACQUIRE, "agent");
;             asm volatile("s_waitcnt vmcnt(0)" ::: "memory");
; __global__ void __launch_bounds__(512, 2) hymba_fwd(Args args) {
;     ...
;             for (int tq = gw; tq < SEQ; tq += 4 * NGW) {
;             int cc0[4], cc1[4];
; #pragma unroll
;             for (int k = 0; k < 4; ++k) { const int t = tq + k * NGW; cc0[k] = 0; cc1[k] = 0; if (t < SEQ) { cc0[k] = tokpos[2 * t]; cc1[k] = tokpos[2 * t + 1]; } }
.LBB0_913:
	s_ashr_i32 s3, s2, 31
	s_lshl_b64 s[0:1], s[2:3], 2
	s_add_u32 s0, s19, s0
	s_addc_u32 s1, s30, s1
	global_load_dwordx2 v[26:27], v48, s[0:1]
	s_cmp_lg_u32 s98, 0
	s_cbranch_scc1 .Lp7gb_passed
	s_mov_b32 s99, 0
	s_cmp_lg_u32 s92, 0
	s_cbranch_scc1 .Lp7gb_follow
	v_mov_b32_e32 v100, 0x22604
	ds_read_b32 v101, v100
	v_mov_b32_e32 v100, 0x3000
	global_load_dword v102, v100, s[26:27] offset:1024 sc1
	s_waitcnt vmcnt(0) lgkmcnt(0)
	v_mul_u32_u24_e32 v101, 6, v101
	s_branch .Lp7gb_chk
.Lp7gb_spin:
	s_sleep 1
	global_load_dword v102, v100, s[26:27] offset:1024 sc1
	s_waitcnt vmcnt(0)
.Lp7gb_chk:
	v_cmp_ge_u32_e32 vcc, v102, v101
	s_cbranch_vccnz .Lp7gb_lead_done
	s_add_i32 s99, s99, 1
	s_cmp_lt_u32 s99, 0x8000
	s_cbranch_scc1 .Lp7gb_spin
.Lp7gb_lead_done:
	buffer_inv sc1
	v_mov_b32_e32 v100, 0x22614
	v_mov_b32_e32 v102, 1
	ds_write_b32 v100, v102
	s_waitcnt vmcnt(0) lgkmcnt(0)
	s_branch .Lp7gb_done
.Lp7gb_follow:
	v_mov_b32_e32 v100, 0x22614
.Lp7gb_fspin:
	ds_read_b32 v102, v100
	s_waitcnt lgkmcnt(0)
	v_cmp_ne_u32_e32 vcc, 0, v102
	s_cbranch_vccnz .Lp7gb_fdone
	s_sleep 1
	s_add_i32 s99, s99, 1
	s_cmp_lt_u32 s99, 0x80000
	s_cbranch_scc1 .Lp7gb_fspin

; #define GAS __attribute__((address_space(1)))
; __global__ void __launch_bounds__(512, 2) hymba_fwd(Args args) {
;     ...
;             for (int k = 0; k < 4; ++k) { const int t = tq + k * NGW; cc0[k] = 0; cc1[k] = 0; if (t < SEQ) { cc0[k] = tokpos[2 * t]; cc1[k] = tokpos[2 * t + 1]; } }
;             v2u xb[2][8]; unsigned b0[2][8], b1[2][8];
;             auto ld = [&](int k) { const int t = tq + k * NGW; const int c0 = cc0[k], c1 = cc1[k];
;                 const size_t r0 = (size_t)(256 * tb[c0 >> 16] + (c0 & 0xffff)), r1 = (size_t)(256 * tb[c1 >> 16] + (c1 & 0xffff));
;                 const GAS v2u* xo = (const GAS v2u*)(X1B + (size_t)t * DM) + lane; const GAS unsigned* y0 = (const GAS unsigned*)((const unsigned char*)Yb + r0 * DM) + lane; const GAS unsigned* y1 = (const GAS unsigned*)((const unsigned char*)Yb + r1 * DM) + lane;
; #pragma unroll
;                 for (int j = 0; j < 8; ++j) { xb[k & 1][j] = __builtin_nontemporal_load(xo + 64 * j); b0[k & 1][j] = __builtin_nontemporal_load(y0 + 64 * j); b1[k & 1][j] = __builtin_nontemporal_load(y1 + 64 * j); } };
.Lp7gb_passed:
	s_add_i32 s0, s90, s34
	s_cmpk_lt_i32 s0, 0x2000
	v_mov_b32_e32 v46, 0
	s_cselect_b64 s[28:29], -1, 0
	s_cmpk_gt_i32 s0, 0x1fff
	v_mov_b32_e32 v47, 0
	s_waitcnt vmcnt(0)
	v_readfirstlane_b32 s1, v26
	v_readfirstlane_b32 s0, v27
	s_cbranch_scc1 .LBB0_915
	s_add_i32 s20, s33, s2
	s_ashr_i32 s21, s20, 31
	s_lshl_b64 s[20:21], s[20:21], 2
	s_add_u32 s20, s19, s20
	s_addc_u32 s21, s30, s21
	global_load_dwordx2 v[46:47], v48, s[20:21]
